# baseline (speedup 1.0000x reference)
.LBB0_34:
	s_andn2_b64 vcc, exec, s[6:7]
	s_cbranch_vccnz .LBB0_41
	s_load_dwordx2 s[10:11], s[0:1], 0x28
	s_movk_i32 s3, 0x300
	v_cmp_gt_u32_e32 vcc, s3, v0
	s_and_saveexec_b64 s[6:7], vcc
	s_cbranch_execz .LBB0_38
	v_lshlrev_b32_e32 v2, 6, v0
	v_mov_b32_e32 v3, 0
	s_waitcnt lgkmcnt(0)
	v_lshl_add_u64 v[4:5], s[8:9], 0, v[2:3]
	s_mov_b64 s[12:13], 0x140000
	v_or_b32_e32 v1, 0xffffff00, v0
	v_lshl_add_u64 v[4:5], v[4:5], 0, s[12:13]
	s_mov_b64 s[12:13], 0
	v_mov_b32_e32 v2, v3
	s_mov_b64 s[14:15], 0x4000
	s_movk_i32 s3, 0x2ff

.LBB5_99:
	s_or_b64 exec, exec, s[18:19]
	s_waitcnt lgkmcnt(0)
	s_barrier
	v_or_b32_e32 v1, s45, v128
	v_cmp_eq_u32_e64 s[8:9], 0, v1
	s_and_saveexec_b64 s[16:17], s[8:9]
	s_cbranch_execz .LBB5_101
	v_mov_b32_e32 v61, 0x23e40
	ds_read_b128 v[42:45], v61
	ds_read_b128 v[46:49], v61 offset:16
	ds_read_b128 v[50:53], v61 offset:32
	ds_read_b128 v[54:57], v61 offset:48
	ds_read_b128 v[58:61], v61 offset:64
	s_lshl_b32 s18, s33, 13
	s_add_u32 s28, s34, s18
	s_addc_u32 s29, s35, 0
	s_ashr_i32 s37, s36, 31
	s_lshl_b64 s[18:19], s[36:37], 6
	s_add_u32 s18, s28, s18
	s_addc_u32 s19, s29, s19
	s_waitcnt lgkmcnt(4)
	v_add_f32_e32 v42, 0, v42
	v_add_f32_e32 v43, 0, v43
	v_add_f32_e32 v42, v42, v44
	v_add_f32_e32 v43, v43, v45
	s_waitcnt lgkmcnt(3)
	v_add_f32_e32 v42, v42, v46
	v_add_f32_e32 v43, v43, v47
	v_add_f32_e32 v42, v42, v48
	v_add_f32_e32 v43, v43, v49
	s_waitcnt lgkmcnt(2)
	v_add_f32_e32 v42, v42, v50
	v_add_f32_e32 v43, v43, v51
	v_add_f32_e32 v42, v42, v52
	v_add_f32_e32 v43, v43, v53
	s_waitcnt lgkmcnt(1)
	v_add_f32_e32 v42, v42, v54
	v_add_f32_e32 v43, v43, v55
	v_add_f32_e32 v42, v42, v56
	v_add_f32_e32 v43, v43, v57
	s_waitcnt lgkmcnt(0)
	v_add_f32_e32 v42, v42, v58
	v_add_f32_e32 v43, v43, v59
	v_add_f32_e32 v42, v42, v60
	v_add_f32_e32 v43, v43, v61
	v_or_b32_e32 v43, 1, v43
	v_mov_b32_e32 v61, 0x140000
	global_store_dwordx2 v61, v[42:43], s[18:19] sc1

.LBB5_107:
	s_cmp_lt_u32 s47, 64
	s_cselect_b64 s[16:17], -1, 0
	s_cmp_gt_u32 s47, 63
	v_cmp_gt_u32_e64 s[10:11], 31, v128
	v_cmp_lt_u32_e64 s[12:13], 30, v128
	v_lshlrev_b32_e32 v82, 6, v128
	s_cbranch_scc1 .LBB5_130
	s_lshl_b32 s18, s33, 13
	s_add_u32 s18, s34, s18
	s_addc_u32 s19, s35, 0
	v_mov_b32_e32 v83, 0
	v_lshl_add_u64 v[2:3], s[18:19], 0, v[82:83]
	s_mov_b64 s[18:19], 0x140000
	v_lshl_add_u64 v[2:3], v[2:3], 0, s[18:19]
	v_mov_b64_e32 v[4:5], 0
	s_mov_b32 s30, 0x400001
	s_mov_b64 s[18:19], 0xffffffff
	s_branch .LBB5_110

.LBB5_141:
	s_or_b64 exec, exec, s[24:25]
	s_waitcnt lgkmcnt(0)
	s_barrier
	s_and_saveexec_b64 s[12:13], s[8:9]
	s_cbranch_execz .LBB5_143
	v_mov_b32_e32 v73, 0x23e40
	ds_read_b128 v[54:57], v73
	ds_read_b128 v[58:61], v73 offset:16
	ds_read_b128 v[62:65], v73 offset:32
	ds_read_b128 v[66:69], v73 offset:48
	ds_read_b128 v[70:73], v73 offset:64
	s_lshl_b32 s18, s33, 13
	s_add_u32 s24, s34, s18
	s_addc_u32 s25, s35, 0
	s_ashr_i32 s37, s36, 31
	s_lshl_b64 s[18:19], s[36:37], 6
	s_add_u32 s18, s24, s18
	s_addc_u32 s19, s25, s19
	s_waitcnt lgkmcnt(4)
	v_add_f32_e32 v54, 0, v54
	v_add_f32_e32 v55, 0, v55
	v_add_f32_e32 v54, v54, v56
	v_add_f32_e32 v55, v55, v57
	s_waitcnt lgkmcnt(3)
	v_add_f32_e32 v54, v54, v58
	v_add_f32_e32 v55, v55, v59
	v_add_f32_e32 v54, v54, v60
	v_add_f32_e32 v55, v55, v61
	s_waitcnt lgkmcnt(2)
	v_add_f32_e32 v54, v54, v62
	v_add_f32_e32 v55, v55, v63
	v_add_f32_e32 v54, v54, v64
	v_add_f32_e32 v55, v55, v65
	s_waitcnt lgkmcnt(1)
	v_add_f32_e32 v54, v54, v66
	v_add_f32_e32 v55, v55, v67
	v_add_f32_e32 v54, v54, v68
	v_add_f32_e32 v55, v55, v69
	s_waitcnt lgkmcnt(0)
	v_add_f32_e32 v54, v54, v70
	v_add_f32_e32 v55, v55, v71
	v_add_f32_e32 v54, v54, v72
	v_add_f32_e32 v55, v55, v73
	v_or_b32_e32 v55, 1, v55
	v_mov_b32_e32 v73, 0x140800
	global_store_dwordx2 v73, v[54:55], s[18:19] sc1

.LBB5_150:
	s_lshl_b32 s10, s33, 13
	s_add_u32 s16, s34, s10
	s_addc_u32 s17, s35, 0
	v_mov_b32_e32 v83, 0
	v_lshl_add_u64 v[0:1], s[16:17], 0, v[82:83]
	s_mov_b64 s[16:17], 0x140800
	v_cmp_gt_u32_e64 s[10:11], 31, v128
	v_cmp_lt_u32_e64 s[12:13], 30, v128
	v_lshl_add_u64 v[0:1], v[0:1], 0, s[16:17]
	v_mov_b64_e32 v[2:3], 0
	s_mov_b32 s24, 0x400001
	s_mov_b64 s[16:17], 0xffffffff
	s_sleep 16
	s_branch .LBB5_152

.LBB5_177:
	s_or_b64 exec, exec, s[14:15]
	s_waitcnt lgkmcnt(0)
	s_barrier
	s_and_saveexec_b64 s[10:11], s[8:9]
	s_cbranch_execz .LBB5_179
	v_mov_b32_e32 v43, 0x23e40
	ds_read_b128 v[24:27], v43
	ds_read_b128 v[28:31], v43 offset:16
	ds_read_b128 v[32:35], v43 offset:32
	ds_read_b128 v[36:39], v43 offset:48
	ds_read_b128 v[40:43], v43 offset:64
	s_waitcnt vmcnt(8)
	s_lshl_b32 s8, s33, 13
	s_add_u32 s12, s34, s8
	s_addc_u32 s13, s35, 0
	s_ashr_i32 s37, s36, 31
	s_lshl_b64 s[8:9], s[36:37], 6
	s_add_u32 s8, s12, s8
	s_addc_u32 s9, s13, s9
	s_waitcnt lgkmcnt(4)
	v_add_f32_e32 v24, 0, v24
	v_add_f32_e32 v25, 0, v25
	v_add_f32_e32 v24, v24, v26
	v_add_f32_e32 v25, v25, v27
	s_waitcnt lgkmcnt(3)
	v_add_f32_e32 v24, v24, v28
	v_add_f32_e32 v25, v25, v29
	v_add_f32_e32 v24, v24, v30
	v_add_f32_e32 v25, v25, v31
	s_waitcnt lgkmcnt(2)
	v_add_f32_e32 v24, v24, v32
	v_add_f32_e32 v25, v25, v33
	v_add_f32_e32 v24, v24, v34
	v_add_f32_e32 v25, v25, v35
	s_waitcnt lgkmcnt(1)
	v_add_f32_e32 v24, v24, v36
	v_add_f32_e32 v25, v25, v37
	v_add_f32_e32 v24, v24, v38
	v_add_f32_e32 v25, v25, v39
	s_waitcnt lgkmcnt(0)
	v_add_f32_e32 v24, v24, v40
	v_add_f32_e32 v25, v25, v41
	v_add_f32_e32 v24, v24, v42
	v_add_f32_e32 v25, v25, v43
	v_or_b32_e32 v25, 1, v25
	v_mov_b32_e32 v43, 0x141000
	global_store_dwordx2 v43, v[24:25], s[8:9] sc1

.LBB5_184:
	s_lshl_b32 s2, s33, 13
	s_add_u32 s8, s34, s2
	s_addc_u32 s9, s35, 0
	v_mov_b32_e32 v83, 0
	s_waitcnt vmcnt(7)
	v_lshl_add_u64 v[36:37], s[8:9], 0, v[82:83]
	s_mov_b64 s[8:9], 0x141000
	v_cmp_gt_u32_e64 s[2:3], 31, v128
	v_cmp_lt_u32_e64 s[4:5], 30, v128
	v_lshl_add_u64 v[36:37], v[36:37], 0, s[8:9]
	s_waitcnt vmcnt(6)
	v_mov_b64_e32 v[38:39], 0
	s_mov_b32 s12, 0x400001
	s_mov_b64 s[8:9], 0xffffffff
	s_sleep 16
	s_branch .LBB5_186
